# GEMM tile heads (P2/P7/P8/P9): 128 accumulators cleared with 64 v_mov_b64 instead of 128 v_mov_b32
# speedup vs baseline: 1.0038x; 1.0038x over previous
.LBB0_246:
	s_ashr_i32 s43, s42, 31
	s_lshl_b64 s[46:47], s[42:43], 19
	s_add_u32 s46, s3, s46
	s_addc_u32 s47, s44, s47
	s_and_b64 s[48:49], s[8:9], exec
	s_cselect_b32 s1, s47, s13
	s_cselect_b32 s2, s46, s12
	s_ashr_i32 s41, s40, 31
	s_lshl_b64 s[48:49], s[40:41], 19
	s_add_u32 s50, s54, s48
	s_addc_u32 s51, s55, s49
	s_and_b64 s[48:49], s[8:9], exec
	s_cselect_b32 s11, s51, s15
	s_cselect_b32 s33, s50, s14
	s_add_u32 s12, s12, 0x40080
	s_addc_u32 s13, s13, 0
	s_add_u32 s41, s14, 0x100
	v_mov_b64_e32 v[2:3], 0
	s_addc_u32 s43, s15, 0
	s_mov_b32 s48, -2
	v_mov_b64_e32 v[4:5], 0
	v_mov_b64_e32 v[6:7], 0
	s_waitcnt lgkmcnt(0)
	v_mov_b64_e32 v[8:9], 0
	v_mov_b64_e32 v[18:19], 0
	v_mov_b64_e32 v[20:21], 0
	v_mov_b64_e32 v[22:23], 0
	v_mov_b64_e32 v[24:25], 0
	v_mov_b64_e32 v[34:35], 0
	v_mov_b64_e32 v[36:37], 0
	v_mov_b64_e32 v[38:39], 0
	v_mov_b64_e32 v[40:41], 0
	v_mov_b64_e32 v[50:51], 0
	v_mov_b64_e32 v[52:53], 0
	v_mov_b64_e32 v[54:55], 0
	v_mov_b64_e32 v[56:57], 0
	v_mov_b64_e32 v[10:11], 0
	v_mov_b64_e32 v[12:13], 0
	v_mov_b64_e32 v[14:15], 0
	v_mov_b64_e32 v[16:17], 0
	v_mov_b64_e32 v[26:27], 0
	v_mov_b64_e32 v[28:29], 0
	v_mov_b64_e32 v[30:31], 0
	v_mov_b64_e32 v[32:33], 0
	v_mov_b64_e32 v[42:43], 0
	v_mov_b64_e32 v[44:45], 0
	v_mov_b64_e32 v[46:47], 0
	v_mov_b64_e32 v[48:49], 0
	v_mov_b64_e32 v[58:59], 0
	v_mov_b64_e32 v[60:61], 0
	v_mov_b64_e32 v[62:63], 0
	v_mov_b64_e32 v[64:65], 0
	v_mov_b64_e32 v[66:67], 0
	v_mov_b64_e32 v[68:69], 0
	v_mov_b64_e32 v[70:71], 0
	v_mov_b64_e32 v[72:73], 0
	v_mov_b64_e32 v[82:83], 0
	v_mov_b64_e32 v[84:85], 0
	v_mov_b64_e32 v[86:87], 0
	v_mov_b64_e32 v[88:89], 0
	v_mov_b64_e32 v[98:99], 0
	v_mov_b64_e32 v[100:101], 0
	v_mov_b64_e32 v[102:103], 0
	v_mov_b64_e32 v[104:105], 0
	v_mov_b64_e32 v[114:115], 0
	v_mov_b64_e32 v[116:117], 0
	v_mov_b64_e32 v[118:119], 0
	v_mov_b64_e32 v[120:121], 0
	v_mov_b64_e32 v[74:75], 0
	v_mov_b64_e32 v[76:77], 0
	v_mov_b64_e32 v[78:79], 0
	v_mov_b64_e32 v[80:81], 0
	v_mov_b64_e32 v[90:91], 0
	v_mov_b64_e32 v[92:93], 0
	v_mov_b64_e32 v[94:95], 0
	v_mov_b64_e32 v[96:97], 0
	v_mov_b64_e32 v[106:107], 0
	v_mov_b64_e32 v[108:109], 0
	v_mov_b64_e32 v[110:111], 0
	v_mov_b64_e32 v[112:113], 0
	v_mov_b64_e32 v[122:123], 0
	v_mov_b64_e32 v[124:125], 0
	v_mov_b64_e32 v[126:127], 0
	v_mov_b64_e32 v[128:129], 0

.LBB0_1639:
	s_ashr_i32 s23, s22, 31
	s_lshl_b64 s[24:25], s[22:23], 19
	s_add_u32 s24, s2, s24
	s_addc_u32 s25, s3, s25
	s_and_b64 s[26:27], s[6:7], exec
	s_cselect_b32 s23, s25, s31
	s_cselect_b32 s29, s24, s30
	s_ashr_i32 s21, s20, 31
	s_lshl_b64 s[26:27], s[20:21], 19
	s_add_u32 s26, s33, s26
	s_addc_u32 s27, s38, s27
	s_and_b64 s[36:37], s[6:7], exec
	s_cselect_b32 s21, s27, s35
	s_cselect_b32 s54, s26, s34
	s_add_u32 s30, s30, 0x40080
	s_addc_u32 s31, s31, 0
	s_add_u32 s55, s34, 0x100
	v_mov_b64_e32 v[2:3], 0
	s_addc_u32 s56, s35, 0
	s_mov_b32 s57, -2
	s_waitcnt lgkmcnt(0)
	v_mov_b64_e32 v[4:5], 0
	v_mov_b64_e32 v[6:7], 0
	v_mov_b64_e32 v[8:9], 0
	v_mov_b64_e32 v[18:19], 0
	v_mov_b64_e32 v[20:21], 0
	v_mov_b64_e32 v[22:23], 0
	v_mov_b64_e32 v[24:25], 0
	v_mov_b64_e32 v[34:35], 0
	v_mov_b64_e32 v[36:37], 0
	v_mov_b64_e32 v[38:39], 0
	v_mov_b64_e32 v[40:41], 0
	v_mov_b64_e32 v[50:51], 0
	v_mov_b64_e32 v[52:53], 0
	v_mov_b64_e32 v[54:55], 0
	v_mov_b64_e32 v[56:57], 0
	v_mov_b64_e32 v[10:11], 0
	v_mov_b64_e32 v[12:13], 0
	v_mov_b64_e32 v[14:15], 0
	v_mov_b64_e32 v[16:17], 0
	v_mov_b64_e32 v[26:27], 0
	v_mov_b64_e32 v[28:29], 0
	v_mov_b64_e32 v[30:31], 0
	v_mov_b64_e32 v[32:33], 0
	v_mov_b64_e32 v[42:43], 0
	v_mov_b64_e32 v[44:45], 0
	v_mov_b64_e32 v[46:47], 0
	v_mov_b64_e32 v[48:49], 0
	v_mov_b64_e32 v[58:59], 0
	v_mov_b64_e32 v[60:61], 0
	v_mov_b64_e32 v[62:63], 0
	v_mov_b64_e32 v[64:65], 0
	v_mov_b64_e32 v[66:67], 0
	v_mov_b64_e32 v[68:69], 0
	v_mov_b64_e32 v[70:71], 0
	v_mov_b64_e32 v[72:73], 0
	v_mov_b64_e32 v[82:83], 0
	v_mov_b64_e32 v[84:85], 0
	v_mov_b64_e32 v[86:87], 0
	v_mov_b64_e32 v[88:89], 0
	v_mov_b64_e32 v[98:99], 0
	v_mov_b64_e32 v[100:101], 0
	v_mov_b64_e32 v[102:103], 0
	v_mov_b64_e32 v[104:105], 0
	v_mov_b64_e32 v[114:115], 0
	v_mov_b64_e32 v[116:117], 0
	v_mov_b64_e32 v[118:119], 0
	v_mov_b64_e32 v[120:121], 0
	v_mov_b64_e32 v[74:75], 0
	v_mov_b64_e32 v[76:77], 0
	v_mov_b64_e32 v[78:79], 0
	v_mov_b64_e32 v[80:81], 0
	v_mov_b64_e32 v[90:91], 0
	v_mov_b64_e32 v[92:93], 0
	v_mov_b64_e32 v[94:95], 0
	v_mov_b64_e32 v[96:97], 0
	v_mov_b64_e32 v[106:107], 0
	v_mov_b64_e32 v[108:109], 0
	v_mov_b64_e32 v[110:111], 0
	v_mov_b64_e32 v[112:113], 0
	v_mov_b64_e32 v[122:123], 0
	v_mov_b64_e32 v[124:125], 0
	v_mov_b64_e32 v[126:127], 0
	v_mov_b64_e32 v[128:129], 0

.LBB0_1740:
	s_ashr_i32 s17, s16, 31
	s_lshl_b64 s[18:19], s[16:17], 19
	s_add_u32 s18, s35, s18
	s_addc_u32 s19, s36, s19
	s_and_b64 s[20:21], s[4:5], exec
	s_cselect_b32 s17, s19, s27
	s_cselect_b32 s23, s18, s26
	s_ashr_i32 s15, s14, 31
	s_lshl_b64 s[20:21], s[14:15], 19
	s_add_u32 s20, s37, s20
	s_addc_u32 s21, s38, s21
	s_and_b64 s[30:31], s[4:5], exec
	s_cselect_b32 s15, s21, s29
	s_cselect_b32 s25, s20, s28
	s_add_u32 s26, s26, 0x40080
	s_addc_u32 s27, s27, 0
	s_add_u32 s54, s28, 0x100
	v_mov_b64_e32 v[2:3], 0
	s_addc_u32 s55, s29, 0
	s_mov_b32 s56, -2
	v_mov_b64_e32 v[4:5], 0
	v_mov_b64_e32 v[6:7], 0
	v_mov_b64_e32 v[8:9], 0
	v_mov_b64_e32 v[18:19], 0
	v_mov_b64_e32 v[20:21], 0
	v_mov_b64_e32 v[22:23], 0
	v_mov_b64_e32 v[24:25], 0
	v_mov_b64_e32 v[34:35], 0
	v_mov_b64_e32 v[36:37], 0
	v_mov_b64_e32 v[38:39], 0
	v_mov_b64_e32 v[40:41], 0
	v_mov_b64_e32 v[50:51], 0
	v_mov_b64_e32 v[52:53], 0
	v_mov_b64_e32 v[54:55], 0
	v_mov_b64_e32 v[56:57], 0
	v_mov_b64_e32 v[10:11], 0
	v_mov_b64_e32 v[12:13], 0
	v_mov_b64_e32 v[14:15], 0
	v_mov_b64_e32 v[16:17], 0
	v_mov_b64_e32 v[26:27], 0
	v_mov_b64_e32 v[28:29], 0
	v_mov_b64_e32 v[30:31], 0
	v_mov_b64_e32 v[32:33], 0
	v_mov_b64_e32 v[42:43], 0
	v_mov_b64_e32 v[44:45], 0
	v_mov_b64_e32 v[46:47], 0
	v_mov_b64_e32 v[48:49], 0
	v_mov_b64_e32 v[66:67], 0
	v_mov_b64_e32 v[68:69], 0
	v_mov_b64_e32 v[70:71], 0
	v_mov_b64_e32 v[72:73], 0
	v_mov_b64_e32 v[82:83], 0
	v_mov_b64_e32 v[84:85], 0
	v_mov_b64_e32 v[86:87], 0
	v_mov_b64_e32 v[88:89], 0
	v_mov_b64_e32 v[98:99], 0
	v_mov_b64_e32 v[100:101], 0
	v_mov_b64_e32 v[102:103], 0
	v_mov_b64_e32 v[104:105], 0
	v_mov_b64_e32 v[114:115], 0
	v_mov_b64_e32 v[116:117], 0
	v_mov_b64_e32 v[118:119], 0
	v_mov_b64_e32 v[120:121], 0
	v_mov_b64_e32 v[130:131], 0
	v_mov_b64_e32 v[132:133], 0
	v_mov_b64_e32 v[134:135], 0
	v_mov_b64_e32 v[136:137], 0
	v_mov_b64_e32 v[90:91], 0
	v_mov_b64_e32 v[92:93], 0
	v_mov_b64_e32 v[94:95], 0
	v_mov_b64_e32 v[96:97], 0
	v_mov_b64_e32 v[106:107], 0
	v_mov_b64_e32 v[108:109], 0
	v_mov_b64_e32 v[110:111], 0
	v_mov_b64_e32 v[112:113], 0
	v_mov_b64_e32 v[122:123], 0
	v_mov_b64_e32 v[124:125], 0
	v_mov_b64_e32 v[126:127], 0
	v_mov_b64_e32 v[128:129], 0
	v_mov_b64_e32 v[138:139], 0
	v_mov_b64_e32 v[140:141], 0
	v_mov_b64_e32 v[142:143], 0
	v_mov_b64_e32 v[144:145], 0

.LBB0_1857:
	s_add_u32 s24, s24, 0xb0080
	s_addc_u32 s25, s25, 0
	s_add_u32 s0, s26, 0x100
	v_mov_b64_e32 v[0:1], 0
	s_addc_u32 s50, s27, 0
	s_mov_b32 s51, -2
	s_waitcnt lgkmcnt(0)
	v_mov_b64_e32 v[2:3], 0
	v_mov_b64_e32 v[4:5], 0
	v_mov_b64_e32 v[6:7], 0
	v_mov_b64_e32 v[16:17], 0
	v_mov_b64_e32 v[18:19], 0
	v_mov_b64_e32 v[20:21], 0
	v_mov_b64_e32 v[22:23], 0
	v_mov_b64_e32 v[32:33], 0
	v_mov_b64_e32 v[34:35], 0
	v_mov_b64_e32 v[36:37], 0
	v_mov_b64_e32 v[38:39], 0
	v_mov_b64_e32 v[48:49], 0
	v_mov_b64_e32 v[50:51], 0
	v_mov_b64_e32 v[52:53], 0
	v_mov_b64_e32 v[54:55], 0
	v_mov_b64_e32 v[8:9], 0
	v_mov_b64_e32 v[10:11], 0
	v_mov_b64_e32 v[12:13], 0
	v_mov_b64_e32 v[14:15], 0
	v_mov_b64_e32 v[24:25], 0
	v_mov_b64_e32 v[26:27], 0
	v_mov_b64_e32 v[28:29], 0
	v_mov_b64_e32 v[30:31], 0
	v_mov_b64_e32 v[40:41], 0
	v_mov_b64_e32 v[42:43], 0
	v_mov_b64_e32 v[44:45], 0
	v_mov_b64_e32 v[46:47], 0
	v_mov_b64_e32 v[56:57], 0
	v_mov_b64_e32 v[58:59], 0
	v_mov_b64_e32 v[60:61], 0
	v_mov_b64_e32 v[62:63], 0
	v_mov_b64_e32 v[64:65], 0
	v_mov_b64_e32 v[66:67], 0
	v_mov_b64_e32 v[68:69], 0
	v_mov_b64_e32 v[70:71], 0
	v_mov_b64_e32 v[80:81], 0
	v_mov_b64_e32 v[82:83], 0
	v_mov_b64_e32 v[84:85], 0
	v_mov_b64_e32 v[86:87], 0
	v_mov_b64_e32 v[96:97], 0
	v_mov_b64_e32 v[98:99], 0
	v_mov_b64_e32 v[100:101], 0
	v_mov_b64_e32 v[102:103], 0
	v_mov_b64_e32 v[112:113], 0
	v_mov_b64_e32 v[114:115], 0
	v_mov_b64_e32 v[116:117], 0
	v_mov_b64_e32 v[118:119], 0
	v_mov_b64_e32 v[72:73], 0
	v_mov_b64_e32 v[74:75], 0
	v_mov_b64_e32 v[76:77], 0
	v_mov_b64_e32 v[78:79], 0
	v_mov_b64_e32 v[88:89], 0
	v_mov_b64_e32 v[90:91], 0
	v_mov_b64_e32 v[92:93], 0
	v_mov_b64_e32 v[94:95], 0
	v_mov_b64_e32 v[104:105], 0
	v_mov_b64_e32 v[106:107], 0
	v_mov_b64_e32 v[108:109], 0
	v_mov_b64_e32 v[110:111], 0
	v_mov_b64_e32 v[120:121], 0
	v_mov_b64_e32 v[122:123], 0
	v_mov_b64_e32 v[124:125], 0
	v_mov_b64_e32 v[126:127], 0
